# drain: both row gathers issued up front with one wait, no store-ack wait between the two outputs; flagged-row index/threshold prefetched before the candidate barrier
# baseline (speedup 1.0000x reference)
.LBB0_102:
	v_lshlrev_b32_e32 v71, 2, v183
	s_waitcnt lgkmcnt(0)
	v_or_b32_e32 v66, 0x213c0, v71
	ds_read_b32 v70, v66
	v_or_b32_e32 v71, 0x21380, v71
	s_movk_i32 s4, 0x3ff0
	ds_read_b32 v71, v71
	ds_read_b128 v[76:79], v175 offset:24576
	ds_read_b128 v[88:91], v174 offset:24576
	s_waitcnt lgkmcnt(3)
	v_lshlrev_b32_e32 v66, 4, v70
	v_and_or_b32 v66, v66, s4, v1
	v_lshlrev_b32_e32 v66, 4, v66
	global_load_dwordx4 v[66:69], v66, s[22:23]
	s_waitcnt lgkmcnt(2)
	v_lshlrev_b32_e32 v80, 4, v71
	v_and_or_b32 v80, v80, s4, v1
	v_lshlrev_b32_e32 v80, 4, v80
	global_load_dwordx4 v[72:75], v80, s[22:23]
	v_or_b32_e32 v92, s24, v183
	s_mov_b32 s4, 0x1e000
	v_lshlrev_b32_e32 v92, 8, v92
	v_or3_b32 v92, v92, v178, s4
	v_or_b32_e32 v93, s24, v173
	v_lshlrev_b32_e32 v93, 8, v93
	v_or3_b32 v93, v93, v178, s4
	v_cmp_lt_i32_e32 vcc, -1, v71
	s_waitcnt vmcnt(0) lgkmcnt(0)
	s_and_saveexec_b64 s[0:1], vcc
	s_cbranch_execz .LBB0_104
	v_pk_add_f32 v[72:73], v[72:73], v[76:77] neg_lo:[0,1] neg_hi:[0,1]
	v_pk_add_f32 v[80:81], v[74:75], v[78:79] neg_lo:[0,1] neg_hi:[0,1]
	v_pk_mul_f32 v[82:83], v[72:73], v[72:73]
	v_pk_add_f32 v[72:73], v[76:77], v[72:73]
	v_pk_add_f32 v[74:75], v[78:79], v[80:81]
	v_pk_mul_f32 v[76:77], v[80:81], v[80:81]
	global_store_dwordx4 v92, v[72:75], s[12:13] sc0 sc1
	v_add_f32_e32 v71, v82, v83
	v_add_f32_e32 v71, v71, v76
	v_add_f32_e32 v71, v71, v77
	v_add_f32_e32 v167, v167, v71
.LBB0_104:
	s_or_b64 exec, exec, s[0:1]
	v_cmp_lt_i32_e32 vcc, -1, v70
	s_and_saveexec_b64 s[0:1], vcc
	s_cbranch_execz .LBB0_106
	v_pk_add_f32 v[66:67], v[66:67], v[88:89] neg_lo:[0,1] neg_hi:[0,1]
	v_pk_add_f32 v[76:77], v[68:69], v[90:91] neg_lo:[0,1] neg_hi:[0,1]
	v_pk_mul_f32 v[74:75], v[66:67], v[66:67]
	v_pk_add_f32 v[66:67], v[88:89], v[66:67]
	v_pk_add_f32 v[68:69], v[90:91], v[76:77]
	global_store_dwordx4 v93, v[66:69], s[12:13] sc0 sc1
	s_nop 1
	v_pk_mul_f32 v[66:67], v[76:77], v[76:77]
	v_add_f32_e32 v68, v74, v75
	v_add_f32_e32 v66, v68, v66
	v_add_f32_e32 v66, v66, v67
	v_add_f32_e32 v167, v167, v66
